# out-projection epilogue rewritten by hand: residual loads prefetched 8 items deep (f32 residual) / all 16 items up front (bf16 residual), scalar-base addressing; same pk_fma + cvt arithmetic
# speedup vs baseline: 1.0048x; 1.0048x over previous
; __device__ __forceinline__ unsigned cvt_pk_bf16(float lo, float hi) { unsigned r; asm volatile("v_cvt_pk_bf16_f32 %0, %1, %2" : "=v"(r) : "v"(lo), "v"(hi)); return r; }
;     __device__ __forceinline__ void operator()(const f32x4 (&acc)[2][2][4][2], const pg8::Unit& u, int wr, int wc, int fr, int fq) const {
;         const int row0 = u.pm * 256 + wr * 64 + fr, col0 = u.pn * 256 + wc * 32 + 8 * fq, b = (u.pm * 256) / S;
;         f32x4 gv[2][2];
; #pragma unroll
;         for (int bj = 0; bj < 2; ++bj)
; #pragma unroll
;             for (int n = 0; n < 2; ++n) gv[bj][n] = *(const f32x4*)(gm + (size_t)b * 6144 + col0 + bj * 128 + n * 4);
;     ...
;         constexpr int PF = 4;
;         if (xin32) {
;             f32x4 xq[PF][2];
; #pragma unroll
;             for (int it = 0; it < PF; ++it) { xq[it][0] = __builtin_nontemporal_load((const f32x4*)(xin32 + EO_OFF(it))); xq[it][1] = __builtin_nontemporal_load((const f32x4*)(xin32 + EO_OFF(it) + 4)); }
; #pragma unroll
;             for (int it = 0; it < 16; ++it) {
;                 const int ai = it >> 3, m = (it >> 1) & 3, bj = it & 1;
;                 const f32x4 x0 = xq[it % PF][0], x1 = xq[it % PF][1];
;                 if (it + PF < 16) { xq[it % PF][0] = __builtin_nontemporal_load((const f32x4*)(xin32 + EO_OFF(it + PF))); xq[it % PF][1] = __builtin_nontemporal_load((const f32x4*)(xin32 + EO_OFF(it + PF) + 4)); }
;                 const f32x4 v0 = x0 + gv[bj][0] * acc[ai][bj][m][0], v1 = x1 + gv[bj][1] * acc[ai][bj][m][1];
;                 u32x4 w; w.x = pg8::cvt_pk_bf16(v0[0], v0[1]); w.y = pg8::cvt_pk_bf16(v0[2], v0[3]); w.z = pg8::cvt_pk_bf16(v1[0], v1[1]); w.w = pg8::cvt_pk_bf16(v1[2], v1[3]);
;                 *(u32x4*)(out + EO_OFF(it)) = w;
;             }
.LBB0_720:
	s_ashr_i32 s15, s43, 31
	s_lshr_b32 s15, s15, 28
	s_add_i32 s15, s43, s15
	s_ashr_i32 s15, s15, 4
	s_mul_hi_i32 s17, s15, 0x6000
	s_mulk_i32 s15, 0x6000
	v_lshl_or_b32 v204, s44, 8, v248
	s_add_u32 s22, s36, s15
	s_addc_u32 s23, s37, s17
	v_lshlrev_b32_e32 v205, 2, v204
	s_lshl_b32 s15, s43, 19
	global_load_dwordx4 v[60:63], v205, s[22:23] offset:16
	global_load_dwordx4 v[64:67], v205, s[22:23]
	global_load_dwordx4 v[52:55], v205, s[22:23] offset:528
	global_load_dwordx4 v[56:59], v205, s[22:23] offset:512
	s_add_u32 s26, s50, s15
	s_addc_u32 s27, s51, 0
	v_lshlrev_b32_e32 v207, 1, v204
	v_lshl_add_u32 v206, v1, 12, v205
	v_lshl_add_u32 v207, v1, 11, v207
	s_andn2_b64 vcc, exec, s[12:13]
	s_cbranch_vccnz .Lop_epi_bf16
	s_lshl_b32 s15, s43, 20
	s_add_u32 s24, s8, s15
	s_addc_u32 s25, s9, 0
	s_add_u32 s28, s24, 0x0
	s_addc_u32 s29, s25, 0
	global_load_dwordx4 v[148:151], v206, s[28:29] nt
	global_load_dwordx4 v[152:155], v206, s[28:29] offset:16 nt
	global_load_dwordx4 v[156:159], v206, s[28:29] offset:512 nt
	global_load_dwordx4 v[160:163], v206, s[28:29] offset:528 nt
	s_add_u32 s28, s24, 0x10000
	s_addc_u32 s29, s25, 0
	global_load_dwordx4 v[164:167], v206, s[28:29] nt
	global_load_dwordx4 v[168:171], v206, s[28:29] offset:16 nt
	global_load_dwordx4 v[172:175], v206, s[28:29] offset:512 nt
	global_load_dwordx4 v[176:179], v206, s[28:29] offset:528 nt
	s_add_u32 s28, s24, 0x20000
	s_addc_u32 s29, s25, 0
	global_load_dwordx4 v[180:183], v206, s[28:29] nt
	global_load_dwordx4 v[184:187], v206, s[28:29] offset:16 nt
	global_load_dwordx4 v[208:211], v206, s[28:29] offset:512 nt
	global_load_dwordx4 v[212:215], v206, s[28:29] offset:528 nt
	s_add_u32 s28, s24, 0x30000
	s_addc_u32 s29, s25, 0
	global_load_dwordx4 v[216:219], v206, s[28:29] nt
	global_load_dwordx4 v[220:223], v206, s[28:29] offset:16 nt
	global_load_dwordx4 v[224:227], v206, s[28:29] offset:512 nt
	global_load_dwordx4 v[228:231], v206, s[28:29] offset:528 nt
	s_add_u32 s32, s26, 0x0
	s_addc_u32 s33, s27, 0
	s_add_u32 s28, s24, 0x80000
	s_addc_u32 s29, s25, 0
	s_waitcnt vmcnt(14)
	v_pk_fma_f32 v[148:149], v[144:145], v[64:65], v[148:149]
	v_pk_fma_f32 v[150:151], v[146:147], v[66:67], v[150:151]
	v_pk_fma_f32 v[152:153], v[140:141], v[60:61], v[152:153]
	v_pk_fma_f32 v[154:155], v[142:143], v[62:63], v[154:155]
	v_cvt_pk_bf16_f32 v148, v148, v149
	v_cvt_pk_bf16_f32 v149, v150, v151
	v_cvt_pk_bf16_f32 v150, v152, v153
	v_cvt_pk_bf16_f32 v151, v154, v155
	global_store_dwordx4 v207, v[148:151], s[32:33]
	global_load_dwordx4 v[148:151], v206, s[28:29] nt
	global_load_dwordx4 v[152:155], v206, s[28:29] offset:16 nt
	s_waitcnt vmcnt(15)
	v_pk_fma_f32 v[156:157], v[136:137], v[56:57], v[156:157]
	v_pk_fma_f32 v[158:159], v[138:139], v[58:59], v[158:159]
	v_pk_fma_f32 v[160:161], v[132:133], v[52:53], v[160:161]
	v_pk_fma_f32 v[162:163], v[134:135], v[54:55], v[162:163]
	v_cvt_pk_bf16_f32 v156, v156, v157
	v_cvt_pk_bf16_f32 v157, v158, v159
	v_cvt_pk_bf16_f32 v158, v160, v161
	v_cvt_pk_bf16_f32 v159, v162, v163
	global_store_dwordx4 v207, v[156:159], s[32:33] offset:256
	global_load_dwordx4 v[156:159], v206, s[28:29] offset:512 nt
	global_load_dwordx4 v[160:163], v206, s[28:29] offset:528 nt
	s_add_u32 s32, s26, 0x8000
	s_addc_u32 s33, s27, 0
	s_add_u32 s28, s24, 0x90000
	s_addc_u32 s29, s25, 0
	s_waitcnt vmcnt(16)
	v_pk_fma_f32 v[164:165], v[128:129], v[64:65], v[164:165]
	v_pk_fma_f32 v[166:167], v[130:131], v[66:67], v[166:167]
	v_pk_fma_f32 v[168:169], v[124:125], v[60:61], v[168:169]
	v_pk_fma_f32 v[170:171], v[126:127], v[62:63], v[170:171]
	v_cvt_pk_bf16_f32 v164, v164, v165
	v_cvt_pk_bf16_f32 v165, v166, v167
	v_cvt_pk_bf16_f32 v166, v168, v169
	v_cvt_pk_bf16_f32 v167, v170, v171
	global_store_dwordx4 v207, v[164:167], s[32:33]
	global_load_dwordx4 v[164:167], v206, s[28:29] nt
	global_load_dwordx4 v[168:171], v206, s[28:29] offset:16 nt
	s_waitcnt vmcnt(17)
	v_pk_fma_f32 v[172:173], v[120:121], v[56:57], v[172:173]
	v_pk_fma_f32 v[174:175], v[122:123], v[58:59], v[174:175]
	v_pk_fma_f32 v[176:177], v[116:117], v[52:53], v[176:177]
	v_pk_fma_f32 v[178:179], v[118:119], v[54:55], v[178:179]
	v_cvt_pk_bf16_f32 v172, v172, v173
	v_cvt_pk_bf16_f32 v173, v174, v175
	v_cvt_pk_bf16_f32 v174, v176, v177
	v_cvt_pk_bf16_f32 v175, v178, v179
	global_store_dwordx4 v207, v[172:175], s[32:33] offset:256
	global_load_dwordx4 v[172:175], v206, s[28:29] offset:512 nt
	global_load_dwordx4 v[176:179], v206, s[28:29] offset:528 nt
	s_add_u32 s32, s26, 0x10000
	s_addc_u32 s33, s27, 0
	s_add_u32 s28, s24, 0xa0000
	s_addc_u32 s29, s25, 0
	s_waitcnt vmcnt(18)
	v_pk_fma_f32 v[180:181], v[112:113], v[64:65], v[180:181]
	v_pk_fma_f32 v[182:183], v[114:115], v[66:67], v[182:183]
	v_pk_fma_f32 v[184:185], v[108:109], v[60:61], v[184:185]
	v_pk_fma_f32 v[186:187], v[110:111], v[62:63], v[186:187]
	v_cvt_pk_bf16_f32 v180, v180, v181
	v_cvt_pk_bf16_f32 v181, v182, v183
	v_cvt_pk_bf16_f32 v182, v184, v185
	v_cvt_pk_bf16_f32 v183, v186, v187
	global_store_dwordx4 v207, v[180:183], s[32:33]
	global_load_dwordx4 v[180:183], v206, s[28:29] nt
	global_load_dwordx4 v[184:187], v206, s[28:29] offset:16 nt
	s_waitcnt vmcnt(19)
	v_pk_fma_f32 v[208:209], v[104:105], v[56:57], v[208:209]
	v_pk_fma_f32 v[210:211], v[106:107], v[58:59], v[210:211]
	v_pk_fma_f32 v[212:213], v[100:101], v[52:53], v[212:213]
	v_pk_fma_f32 v[214:215], v[102:103], v[54:55], v[214:215]
	v_cvt_pk_bf16_f32 v208, v208, v209
	v_cvt_pk_bf16_f32 v209, v210, v211
	v_cvt_pk_bf16_f32 v210, v212, v213
	v_cvt_pk_bf16_f32 v211, v214, v215
	global_store_dwordx4 v207, v[208:211], s[32:33] offset:256
	global_load_dwordx4 v[208:211], v206, s[28:29] offset:512 nt
	global_load_dwordx4 v[212:215], v206, s[28:29] offset:528 nt
	s_add_u32 s32, s26, 0x18000
	s_addc_u32 s33, s27, 0
	s_add_u32 s28, s24, 0xb0000
	s_addc_u32 s29, s25, 0
	s_waitcnt vmcnt(20)
; __device__ __forceinline__ unsigned cvt_pk_bf16(float lo, float hi) { unsigned r; asm volatile("v_cvt_pk_bf16_f32 %0, %1, %2" : "=v"(r) : "v"(lo), "v"(hi)); return r; }
;     __device__ __forceinline__ void operator()(const f32x4 (&acc)[2][2][4][2], const pg8::Unit& u, int wr, int wc, int fr, int fq) const {
;     ...
;         if (xin32) {
;             f32x4 xq[PF][2];
; #pragma unroll
;             for (int it = 0; it < PF; ++it) { xq[it][0] = __builtin_nontemporal_load((const f32x4*)(xin32 + EO_OFF(it))); xq[it][1] = __builtin_nontemporal_load((const f32x4*)(xin32 + EO_OFF(it) + 4)); }
; #pragma unroll
;             for (int it = 0; it < 16; ++it) {
;                 const int ai = it >> 3, m = (it >> 1) & 3, bj = it & 1;
;                 const f32x4 x0 = xq[it % PF][0], x1 = xq[it % PF][1];
;                 if (it + PF < 16) { xq[it % PF][0] = __builtin_nontemporal_load((const f32x4*)(xin32 + EO_OFF(it + PF))); xq[it % PF][1] = __builtin_nontemporal_load((const f32x4*)(xin32 + EO_OFF(it + PF) + 4)); }
;                 const f32x4 v0 = x0 + gv[bj][0] * acc[ai][bj][m][0], v1 = x1 + gv[bj][1] * acc[ai][bj][m][1];
;                 u32x4 w; w.x = pg8::cvt_pk_bf16(v0[0], v0[1]); w.y = pg8::cvt_pk_bf16(v0[2], v0[3]); w.z = pg8::cvt_pk_bf16(v1[0], v1[1]); w.w = pg8::cvt_pk_bf16(v1[2], v1[3]);
;                 *(u32x4*)(out + EO_OFF(it)) = w;
;             }
	v_pk_fma_f32 v[216:217], v[96:97], v[64:65], v[216:217]
	v_pk_fma_f32 v[218:219], v[98:99], v[66:67], v[218:219]
	v_pk_fma_f32 v[220:221], v[92:93], v[60:61], v[220:221]
	v_pk_fma_f32 v[222:223], v[94:95], v[62:63], v[222:223]
	v_cvt_pk_bf16_f32 v216, v216, v217
	v_cvt_pk_bf16_f32 v217, v218, v219
	v_cvt_pk_bf16_f32 v218, v220, v221
	v_cvt_pk_bf16_f32 v219, v222, v223
	global_store_dwordx4 v207, v[216:219], s[32:33]
	global_load_dwordx4 v[216:219], v206, s[28:29] nt
	global_load_dwordx4 v[220:223], v206, s[28:29] offset:16 nt
	s_waitcnt vmcnt(21)
	v_pk_fma_f32 v[224:225], v[88:89], v[56:57], v[224:225]
	v_pk_fma_f32 v[226:227], v[90:91], v[58:59], v[226:227]
	v_pk_fma_f32 v[228:229], v[84:85], v[52:53], v[228:229]
	v_pk_fma_f32 v[230:231], v[86:87], v[54:55], v[230:231]
	v_cvt_pk_bf16_f32 v224, v224, v225
	v_cvt_pk_bf16_f32 v225, v226, v227
	v_cvt_pk_bf16_f32 v226, v228, v229
	v_cvt_pk_bf16_f32 v227, v230, v231
	global_store_dwordx4 v207, v[224:227], s[32:33] offset:256
	global_load_dwordx4 v[224:227], v206, s[28:29] offset:512 nt
	global_load_dwordx4 v[228:231], v206, s[28:29] offset:528 nt
	s_add_u32 s32, s26, 0x40000
	s_addc_u32 s33, s27, 0
	s_waitcnt vmcnt(21)
	v_pk_fma_f32 v[148:149], v[80:81], v[64:65], v[148:149]
	v_pk_fma_f32 v[150:151], v[82:83], v[66:67], v[150:151]
	v_pk_fma_f32 v[152:153], v[76:77], v[60:61], v[152:153]
	v_pk_fma_f32 v[154:155], v[78:79], v[62:63], v[154:155]
	v_cvt_pk_bf16_f32 v148, v148, v149
	v_cvt_pk_bf16_f32 v149, v150, v151
	v_cvt_pk_bf16_f32 v150, v152, v153
	v_cvt_pk_bf16_f32 v151, v154, v155
	global_store_dwordx4 v207, v[148:151], s[32:33]
	s_waitcnt vmcnt(19)
	v_pk_fma_f32 v[156:157], v[72:73], v[56:57], v[156:157]
	v_pk_fma_f32 v[158:159], v[74:75], v[58:59], v[158:159]
	v_pk_fma_f32 v[160:161], v[68:69], v[52:53], v[160:161]
	v_pk_fma_f32 v[162:163], v[70:71], v[54:55], v[162:163]
	v_cvt_pk_bf16_f32 v156, v156, v157
	v_cvt_pk_bf16_f32 v157, v158, v159
	v_cvt_pk_bf16_f32 v158, v160, v161
	v_cvt_pk_bf16_f32 v159, v162, v163
	global_store_dwordx4 v207, v[156:159], s[32:33] offset:256
	s_add_u32 s32, s26, 0x48000
	s_addc_u32 s33, s27, 0
	s_waitcnt vmcnt(17)
	v_pk_fma_f32 v[164:165], v[48:49], v[64:65], v[164:165]
	v_pk_fma_f32 v[166:167], v[50:51], v[66:67], v[166:167]
	v_pk_fma_f32 v[168:169], v[44:45], v[60:61], v[168:169]
	v_pk_fma_f32 v[170:171], v[46:47], v[62:63], v[170:171]
	v_cvt_pk_bf16_f32 v164, v164, v165
	v_cvt_pk_bf16_f32 v165, v166, v167
	v_cvt_pk_bf16_f32 v166, v168, v169
	v_cvt_pk_bf16_f32 v167, v170, v171
	global_store_dwordx4 v207, v[164:167], s[32:33]
	s_waitcnt vmcnt(15)
	v_pk_fma_f32 v[172:173], v[40:41], v[56:57], v[172:173]
	v_pk_fma_f32 v[174:175], v[42:43], v[58:59], v[174:175]
	v_pk_fma_f32 v[176:177], v[36:37], v[52:53], v[176:177]
	v_pk_fma_f32 v[178:179], v[38:39], v[54:55], v[178:179]
	v_cvt_pk_bf16_f32 v172, v172, v173
	v_cvt_pk_bf16_f32 v173, v174, v175
	v_cvt_pk_bf16_f32 v174, v176, v177
	v_cvt_pk_bf16_f32 v175, v178, v179
	global_store_dwordx4 v207, v[172:175], s[32:33] offset:256
	s_add_u32 s32, s26, 0x50000
	s_addc_u32 s33, s27, 0
	s_waitcnt vmcnt(13)
	v_pk_fma_f32 v[180:181], v[30:31], v[64:65], v[180:181]
	v_pk_fma_f32 v[182:183], v[32:33], v[66:67], v[182:183]
	v_pk_fma_f32 v[184:185], v[26:27], v[60:61], v[184:185]
	v_pk_fma_f32 v[186:187], v[28:29], v[62:63], v[186:187]
	v_cvt_pk_bf16_f32 v180, v180, v181
	v_cvt_pk_bf16_f32 v181, v182, v183
	v_cvt_pk_bf16_f32 v182, v184, v185
	v_cvt_pk_bf16_f32 v183, v186, v187
	global_store_dwordx4 v207, v[180:183], s[32:33]
	s_waitcnt vmcnt(11)
	v_pk_fma_f32 v[208:209], v[22:23], v[56:57], v[208:209]
	v_pk_fma_f32 v[210:211], v[24:25], v[58:59], v[210:211]
	v_pk_fma_f32 v[212:213], v[18:19], v[52:53], v[212:213]
	v_pk_fma_f32 v[214:215], v[20:21], v[54:55], v[214:215]
	v_cvt_pk_bf16_f32 v208, v208, v209
	v_cvt_pk_bf16_f32 v209, v210, v211
	v_cvt_pk_bf16_f32 v210, v212, v213
	v_cvt_pk_bf16_f32 v211, v214, v215
	global_store_dwordx4 v207, v[208:211], s[32:33] offset:256
	s_add_u32 s32, s26, 0x58000
	s_addc_u32 s33, s27, 0
	s_waitcnt vmcnt(9)
	v_pk_fma_f32 v[216:217], v[14:15], v[64:65], v[216:217]
	v_pk_fma_f32 v[218:219], v[16:17], v[66:67], v[218:219]
	v_pk_fma_f32 v[220:221], v[10:11], v[60:61], v[220:221]
	v_pk_fma_f32 v[222:223], v[12:13], v[62:63], v[222:223]
	v_cvt_pk_bf16_f32 v216, v216, v217
	v_cvt_pk_bf16_f32 v217, v218, v219
	v_cvt_pk_bf16_f32 v218, v220, v221
	v_cvt_pk_bf16_f32 v219, v222, v223
	global_store_dwordx4 v207, v[216:219], s[32:33]
	s_waitcnt vmcnt(7)
	v_pk_fma_f32 v[224:225], v[6:7], v[56:57], v[224:225]
	v_pk_fma_f32 v[226:227], v[8:9], v[58:59], v[226:227]
	v_pk_fma_f32 v[228:229], v[2:3], v[52:53], v[228:229]
	v_pk_fma_f32 v[230:231], v[4:5], v[54:55], v[230:231]
	v_cvt_pk_bf16_f32 v224, v224, v225
	v_cvt_pk_bf16_f32 v225, v226, v227
	v_cvt_pk_bf16_f32 v226, v228, v229
	v_cvt_pk_bf16_f32 v227, v230, v231
	global_store_dwordx4 v207, v[224:227], s[32:33] offset:256
	s_branch .Lop_epi_done
; __device__ __forceinline__ unsigned cvt_pk_bf16(float lo, float hi) { unsigned r; asm volatile("v_cvt_pk_bf16_f32 %0, %1, %2" : "=v"(r) : "v"(lo), "v"(hi)); return r; }
;     __device__ __forceinline__ void operator()(const f32x4 (&acc)[2][2][4][2], const pg8::Unit& u, int wr, int wc, int fr, int fq) const {
;     ...
;             u32x4 xq[PF];
; #pragma unroll
;             for (int it = 0; it < PF; ++it) xq[it] = __builtin_nontemporal_load((const u32x4*)(xin16 + EO_OFF(it)));
; #pragma unroll
;             for (int it = 0; it < 16; ++it) {
;                 const int ai = it >> 3, m = (it >> 1) & 3, bj = it & 1;
;                 const u32x4 xv = xq[it % PF];
;                 if (it + PF < 16) xq[it % PF] = __builtin_nontemporal_load((const u32x4*)(xin16 + EO_OFF(it + PF)));
;                 const f32x4 x0 = (f32x4){__uint_as_float(xv.x << 16), __uint_as_float(xv.x & 0xffff0000u), __uint_as_float(xv.y << 16), __uint_as_float(xv.y & 0xffff0000u)};
;                 const f32x4 x1 = (f32x4){__uint_as_float(xv.z << 16), __uint_as_float(xv.z & 0xffff0000u), __uint_as_float(xv.w << 16), __uint_as_float(xv.w & 0xffff0000u)};
;                 const f32x4 v0 = x0 + gv[bj][0] * acc[ai][bj][m][0], v1 = x1 + gv[bj][1] * acc[ai][bj][m][1];
;                 u32x4 w; w.x = pg8::cvt_pk_bf16(v0[0], v0[1]); w.y = pg8::cvt_pk_bf16(v0[2], v0[3]); w.z = pg8::cvt_pk_bf16(v1[0], v1[1]); w.w = pg8::cvt_pk_bf16(v1[2], v1[3]);
;                 *(u32x4*)(out + EO_OFF(it)) = w;
;             }
.Lop_epi_bf16:
	s_add_u32 s28, s26, 0x0
	s_addc_u32 s29, s27, 0
	global_load_dwordx4 v[148:151], v207, s[28:29] nt
	global_load_dwordx4 v[152:155], v207, s[28:29] offset:256 nt
	s_add_u32 s28, s26, 0x8000
	s_addc_u32 s29, s27, 0
	global_load_dwordx4 v[156:159], v207, s[28:29] nt
	global_load_dwordx4 v[160:163], v207, s[28:29] offset:256 nt
	s_add_u32 s28, s26, 0x10000
	s_addc_u32 s29, s27, 0
	global_load_dwordx4 v[164:167], v207, s[28:29] nt
	global_load_dwordx4 v[168:171], v207, s[28:29] offset:256 nt
	s_add_u32 s28, s26, 0x18000
	s_addc_u32 s29, s27, 0
	global_load_dwordx4 v[172:175], v207, s[28:29] nt
	global_load_dwordx4 v[176:179], v207, s[28:29] offset:256 nt
	s_add_u32 s28, s26, 0x40000
	s_addc_u32 s29, s27, 0
	global_load_dwordx4 v[180:183], v207, s[28:29] nt
	global_load_dwordx4 v[184:187], v207, s[28:29] offset:256 nt
	s_add_u32 s28, s26, 0x48000
	s_addc_u32 s29, s27, 0
	global_load_dwordx4 v[208:211], v207, s[28:29] nt
	global_load_dwordx4 v[212:215], v207, s[28:29] offset:256 nt
	s_add_u32 s28, s26, 0x50000
	s_addc_u32 s29, s27, 0
	global_load_dwordx4 v[216:219], v207, s[28:29] nt
	global_load_dwordx4 v[220:223], v207, s[28:29] offset:256 nt
	s_add_u32 s28, s26, 0x58000
	s_addc_u32 s29, s27, 0
	global_load_dwordx4 v[224:227], v207, s[28:29] nt
	global_load_dwordx4 v[228:231], v207, s[28:29] offset:256 nt
	s_add_u32 s32, s26, 0x0
	s_addc_u32 s33, s27, 0
	s_waitcnt vmcnt(15)
	v_lshlrev_b32_e32 v232, 16, v148
	v_and_b32_e32 v233, 0xffff0000, v148
	v_lshlrev_b32_e32 v234, 16, v149
	v_and_b32_e32 v235, 0xffff0000, v149
	v_lshlrev_b32_e32 v244, 16, v150
	v_and_b32_e32 v245, 0xffff0000, v150
	v_lshlrev_b32_e32 v246, 16, v151
	v_and_b32_e32 v247, 0xffff0000, v151
	v_pk_fma_f32 v[144:145], v[144:145], v[64:65], v[232:233]
	v_pk_fma_f32 v[146:147], v[146:147], v[66:67], v[234:235]
	v_pk_fma_f32 v[140:141], v[140:141], v[60:61], v[244:245]
	v_pk_fma_f32 v[142:143], v[142:143], v[62:63], v[246:247]
	v_cvt_pk_bf16_f32 v148, v144, v145
	v_cvt_pk_bf16_f32 v149, v146, v147
	v_cvt_pk_bf16_f32 v150, v140, v141
	v_cvt_pk_bf16_f32 v151, v142, v143
	global_store_dwordx4 v207, v[148:151], s[32:33]
	s_waitcnt vmcnt(15)
	v_lshlrev_b32_e32 v232, 16, v152
	v_and_b32_e32 v233, 0xffff0000, v152
	v_lshlrev_b32_e32 v234, 16, v153
	v_and_b32_e32 v235, 0xffff0000, v153
	v_lshlrev_b32_e32 v244, 16, v154
	v_and_b32_e32 v245, 0xffff0000, v154
	v_lshlrev_b32_e32 v246, 16, v155
	v_and_b32_e32 v247, 0xffff0000, v155
	v_pk_fma_f32 v[136:137], v[136:137], v[56:57], v[232:233]
	v_pk_fma_f32 v[138:139], v[138:139], v[58:59], v[234:235]
	v_pk_fma_f32 v[132:133], v[132:133], v[52:53], v[244:245]
	v_pk_fma_f32 v[134:135], v[134:135], v[54:55], v[246:247]
	v_cvt_pk_bf16_f32 v152, v136, v137
	v_cvt_pk_bf16_f32 v153, v138, v139
	v_cvt_pk_bf16_f32 v154, v132, v133
	v_cvt_pk_bf16_f32 v155, v134, v135
	global_store_dwordx4 v207, v[152:155], s[32:33] offset:256
	s_add_u32 s32, s26, 0x8000
	s_addc_u32 s33, s27, 0
	s_waitcnt vmcnt(15)
	v_lshlrev_b32_e32 v232, 16, v156
	v_and_b32_e32 v233, 0xffff0000, v156
	v_lshlrev_b32_e32 v234, 16, v157
	v_and_b32_e32 v235, 0xffff0000, v157
	v_lshlrev_b32_e32 v244, 16, v158
	v_and_b32_e32 v245, 0xffff0000, v158
	v_lshlrev_b32_e32 v246, 16, v159
	v_and_b32_e32 v247, 0xffff0000, v159
	v_pk_fma_f32 v[128:129], v[128:129], v[64:65], v[232:233]
	v_pk_fma_f32 v[130:131], v[130:131], v[66:67], v[234:235]
	v_pk_fma_f32 v[124:125], v[124:125], v[60:61], v[244:245]
	v_pk_fma_f32 v[126:127], v[126:127], v[62:63], v[246:247]
	v_cvt_pk_bf16_f32 v156, v128, v129
	v_cvt_pk_bf16_f32 v157, v130, v131
	v_cvt_pk_bf16_f32 v158, v124, v125
	v_cvt_pk_bf16_f32 v159, v126, v127
	global_store_dwordx4 v207, v[156:159], s[32:33]
	s_waitcnt vmcnt(15)
	v_lshlrev_b32_e32 v232, 16, v160
	v_and_b32_e32 v233, 0xffff0000, v160
	v_lshlrev_b32_e32 v234, 16, v161
	v_and_b32_e32 v235, 0xffff0000, v161
	v_lshlrev_b32_e32 v244, 16, v162
	v_and_b32_e32 v245, 0xffff0000, v162
	v_lshlrev_b32_e32 v246, 16, v163
	v_and_b32_e32 v247, 0xffff0000, v163
	v_pk_fma_f32 v[120:121], v[120:121], v[56:57], v[232:233]
	v_pk_fma_f32 v[122:123], v[122:123], v[58:59], v[234:235]
	v_pk_fma_f32 v[116:117], v[116:117], v[52:53], v[244:245]
	v_pk_fma_f32 v[118:119], v[118:119], v[54:55], v[246:247]
	v_cvt_pk_bf16_f32 v160, v120, v121
	v_cvt_pk_bf16_f32 v161, v122, v123
	v_cvt_pk_bf16_f32 v162, v116, v117
	v_cvt_pk_bf16_f32 v163, v118, v119
	global_store_dwordx4 v207, v[160:163], s[32:33] offset:256
	s_add_u32 s32, s26, 0x10000
	s_addc_u32 s33, s27, 0
	s_waitcnt vmcnt(15)
	v_lshlrev_b32_e32 v232, 16, v164
	v_and_b32_e32 v233, 0xffff0000, v164
	v_lshlrev_b32_e32 v234, 16, v165
	v_and_b32_e32 v235, 0xffff0000, v165
	v_lshlrev_b32_e32 v244, 16, v166
	v_and_b32_e32 v245, 0xffff0000, v166
	v_lshlrev_b32_e32 v246, 16, v167
	v_and_b32_e32 v247, 0xffff0000, v167
	v_pk_fma_f32 v[112:113], v[112:113], v[64:65], v[232:233]
	v_pk_fma_f32 v[114:115], v[114:115], v[66:67], v[234:235]
	v_pk_fma_f32 v[108:109], v[108:109], v[60:61], v[244:245]
	v_pk_fma_f32 v[110:111], v[110:111], v[62:63], v[246:247]
	v_cvt_pk_bf16_f32 v164, v112, v113
	v_cvt_pk_bf16_f32 v165, v114, v115
	v_cvt_pk_bf16_f32 v166, v108, v109
	v_cvt_pk_bf16_f32 v167, v110, v111
	global_store_dwordx4 v207, v[164:167], s[32:33]
	s_waitcnt vmcnt(15)
	v_lshlrev_b32_e32 v232, 16, v168
	v_and_b32_e32 v233, 0xffff0000, v168
	v_lshlrev_b32_e32 v234, 16, v169
	v_and_b32_e32 v235, 0xffff0000, v169
	v_lshlrev_b32_e32 v244, 16, v170
	v_and_b32_e32 v245, 0xffff0000, v170
	v_lshlrev_b32_e32 v246, 16, v171
	v_and_b32_e32 v247, 0xffff0000, v171
	v_pk_fma_f32 v[104:105], v[104:105], v[56:57], v[232:233]
	v_pk_fma_f32 v[106:107], v[106:107], v[58:59], v[234:235]
	v_pk_fma_f32 v[100:101], v[100:101], v[52:53], v[244:245]
	v_pk_fma_f32 v[102:103], v[102:103], v[54:55], v[246:247]
	v_cvt_pk_bf16_f32 v168, v104, v105
	v_cvt_pk_bf16_f32 v169, v106, v107
	v_cvt_pk_bf16_f32 v170, v100, v101
	v_cvt_pk_bf16_f32 v171, v102, v103
	global_store_dwordx4 v207, v[168:171], s[32:33] offset:256
	s_add_u32 s32, s26, 0x18000
	s_addc_u32 s33, s27, 0
	s_waitcnt vmcnt(15)
; __device__ __forceinline__ unsigned cvt_pk_bf16(float lo, float hi) { unsigned r; asm volatile("v_cvt_pk_bf16_f32 %0, %1, %2" : "=v"(r) : "v"(lo), "v"(hi)); return r; }
;     __device__ __forceinline__ void operator()(const f32x4 (&acc)[2][2][4][2], const pg8::Unit& u, int wr, int wc, int fr, int fq) const {
;     ...
;             for (int it = 0; it < 16; ++it) {
;                 const int ai = it >> 3, m = (it >> 1) & 3, bj = it & 1;
;                 const u32x4 xv = xq[it % PF];
;                 if (it + PF < 16) xq[it % PF] = __builtin_nontemporal_load((const u32x4*)(xin16 + EO_OFF(it + PF)));
;                 const f32x4 x0 = (f32x4){__uint_as_float(xv.x << 16), __uint_as_float(xv.x & 0xffff0000u), __uint_as_float(xv.y << 16), __uint_as_float(xv.y & 0xffff0000u)};
;                 const f32x4 x1 = (f32x4){__uint_as_float(xv.z << 16), __uint_as_float(xv.z & 0xffff0000u), __uint_as_float(xv.w << 16), __uint_as_float(xv.w & 0xffff0000u)};
;                 const f32x4 v0 = x0 + gv[bj][0] * acc[ai][bj][m][0], v1 = x1 + gv[bj][1] * acc[ai][bj][m][1];
;                 u32x4 w; w.x = pg8::cvt_pk_bf16(v0[0], v0[1]); w.y = pg8::cvt_pk_bf16(v0[2], v0[3]); w.z = pg8::cvt_pk_bf16(v1[0], v1[1]); w.w = pg8::cvt_pk_bf16(v1[2], v1[3]);
;                 *(u32x4*)(out + EO_OFF(it)) = w;
;             }
	v_lshlrev_b32_e32 v232, 16, v172
	v_and_b32_e32 v233, 0xffff0000, v172
	v_lshlrev_b32_e32 v234, 16, v173
	v_and_b32_e32 v235, 0xffff0000, v173
	v_lshlrev_b32_e32 v244, 16, v174
	v_and_b32_e32 v245, 0xffff0000, v174
	v_lshlrev_b32_e32 v246, 16, v175
	v_and_b32_e32 v247, 0xffff0000, v175
	v_pk_fma_f32 v[96:97], v[96:97], v[64:65], v[232:233]
	v_pk_fma_f32 v[98:99], v[98:99], v[66:67], v[234:235]
	v_pk_fma_f32 v[92:93], v[92:93], v[60:61], v[244:245]
	v_pk_fma_f32 v[94:95], v[94:95], v[62:63], v[246:247]
	v_cvt_pk_bf16_f32 v172, v96, v97
	v_cvt_pk_bf16_f32 v173, v98, v99
	v_cvt_pk_bf16_f32 v174, v92, v93
	v_cvt_pk_bf16_f32 v175, v94, v95
	global_store_dwordx4 v207, v[172:175], s[32:33]
	s_waitcnt vmcnt(15)
	v_lshlrev_b32_e32 v232, 16, v176
	v_and_b32_e32 v233, 0xffff0000, v176
	v_lshlrev_b32_e32 v234, 16, v177
	v_and_b32_e32 v235, 0xffff0000, v177
	v_lshlrev_b32_e32 v244, 16, v178
	v_and_b32_e32 v245, 0xffff0000, v178
	v_lshlrev_b32_e32 v246, 16, v179
	v_and_b32_e32 v247, 0xffff0000, v179
	v_pk_fma_f32 v[88:89], v[88:89], v[56:57], v[232:233]
	v_pk_fma_f32 v[90:91], v[90:91], v[58:59], v[234:235]
	v_pk_fma_f32 v[84:85], v[84:85], v[52:53], v[244:245]
	v_pk_fma_f32 v[86:87], v[86:87], v[54:55], v[246:247]
	v_cvt_pk_bf16_f32 v176, v88, v89
	v_cvt_pk_bf16_f32 v177, v90, v91
	v_cvt_pk_bf16_f32 v178, v84, v85
	v_cvt_pk_bf16_f32 v179, v86, v87
	global_store_dwordx4 v207, v[176:179], s[32:33] offset:256
	s_add_u32 s32, s26, 0x40000
	s_addc_u32 s33, s27, 0
	s_waitcnt vmcnt(15)
	v_lshlrev_b32_e32 v232, 16, v180
	v_and_b32_e32 v233, 0xffff0000, v180
	v_lshlrev_b32_e32 v234, 16, v181
	v_and_b32_e32 v235, 0xffff0000, v181
	v_lshlrev_b32_e32 v244, 16, v182
	v_and_b32_e32 v245, 0xffff0000, v182
	v_lshlrev_b32_e32 v246, 16, v183
	v_and_b32_e32 v247, 0xffff0000, v183
	v_pk_fma_f32 v[80:81], v[80:81], v[64:65], v[232:233]
	v_pk_fma_f32 v[82:83], v[82:83], v[66:67], v[234:235]
	v_pk_fma_f32 v[76:77], v[76:77], v[60:61], v[244:245]
	v_pk_fma_f32 v[78:79], v[78:79], v[62:63], v[246:247]
	v_cvt_pk_bf16_f32 v180, v80, v81
	v_cvt_pk_bf16_f32 v181, v82, v83
	v_cvt_pk_bf16_f32 v182, v76, v77
	v_cvt_pk_bf16_f32 v183, v78, v79
	global_store_dwordx4 v207, v[180:183], s[32:33]
	s_waitcnt vmcnt(15)
	v_lshlrev_b32_e32 v232, 16, v184
	v_and_b32_e32 v233, 0xffff0000, v184
	v_lshlrev_b32_e32 v234, 16, v185
	v_and_b32_e32 v235, 0xffff0000, v185
	v_lshlrev_b32_e32 v244, 16, v186
	v_and_b32_e32 v245, 0xffff0000, v186
	v_lshlrev_b32_e32 v246, 16, v187
	v_and_b32_e32 v247, 0xffff0000, v187
	v_pk_fma_f32 v[72:73], v[72:73], v[56:57], v[232:233]
	v_pk_fma_f32 v[74:75], v[74:75], v[58:59], v[234:235]
	v_pk_fma_f32 v[68:69], v[68:69], v[52:53], v[244:245]
	v_pk_fma_f32 v[70:71], v[70:71], v[54:55], v[246:247]
	v_cvt_pk_bf16_f32 v184, v72, v73
	v_cvt_pk_bf16_f32 v185, v74, v75
	v_cvt_pk_bf16_f32 v186, v68, v69
	v_cvt_pk_bf16_f32 v187, v70, v71
	global_store_dwordx4 v207, v[184:187], s[32:33] offset:256
	s_add_u32 s32, s26, 0x48000
	s_addc_u32 s33, s27, 0
	s_waitcnt vmcnt(15)
	v_lshlrev_b32_e32 v232, 16, v208
	v_and_b32_e32 v233, 0xffff0000, v208
	v_lshlrev_b32_e32 v234, 16, v209
	v_and_b32_e32 v235, 0xffff0000, v209
	v_lshlrev_b32_e32 v244, 16, v210
	v_and_b32_e32 v245, 0xffff0000, v210
	v_lshlrev_b32_e32 v246, 16, v211
	v_and_b32_e32 v247, 0xffff0000, v211
	v_pk_fma_f32 v[48:49], v[48:49], v[64:65], v[232:233]
	v_pk_fma_f32 v[50:51], v[50:51], v[66:67], v[234:235]
	v_pk_fma_f32 v[44:45], v[44:45], v[60:61], v[244:245]
	v_pk_fma_f32 v[46:47], v[46:47], v[62:63], v[246:247]
	v_cvt_pk_bf16_f32 v208, v48, v49
	v_cvt_pk_bf16_f32 v209, v50, v51
	v_cvt_pk_bf16_f32 v210, v44, v45
	v_cvt_pk_bf16_f32 v211, v46, v47
	global_store_dwordx4 v207, v[208:211], s[32:33]
	s_waitcnt vmcnt(15)
; __device__ __forceinline__ unsigned cvt_pk_bf16(float lo, float hi) { unsigned r; asm volatile("v_cvt_pk_bf16_f32 %0, %1, %2" : "=v"(r) : "v"(lo), "v"(hi)); return r; }
; #define PG8_BAR __builtin_amdgcn_s_barrier()
; #define PG8_BAR __builtin_amdgcn_s_barrier()
;     ...
;         if (wr == 0) PG8_BAR;
;         E(acc, cur, wr, wc, fr, fq);
;         if (!has_next) break;
; #pragma unroll
;         for (int a = 0; a < 2; ++a)
; #pragma unroll
;             for (int b = 0; b < 2; ++b)
; #pragma unroll
;                 for (int m = 0; m < 4; ++m)
; #pragma unroll
;                     for (int n = 0; n < 2; ++n) acc[a][b][m][n] = (f32x4){0.f, 0.f, 0.f, 0.f};
;         cur = nxt; cA = nA; cB = nB; ++ui;
;         if (wr == 1) PG8_BAR;
;     }
;     __device__ __forceinline__ void operator()(const f32x4 (&acc)[2][2][4][2], const pg8::Unit& u, int wr, int wc, int fr, int fq) const {
;     ...
;             for (int it = 0; it < 16; ++it) {
;                 const int ai = it >> 3, m = (it >> 1) & 3, bj = it & 1;
;                 const u32x4 xv = xq[it % PF];
;                 if (it + PF < 16) xq[it % PF] = __builtin_nontemporal_load((const u32x4*)(xin16 + EO_OFF(it + PF)));
;                 const f32x4 x0 = (f32x4){__uint_as_float(xv.x << 16), __uint_as_float(xv.x & 0xffff0000u), __uint_as_float(xv.y << 16), __uint_as_float(xv.y & 0xffff0000u)};
;                 const f32x4 x1 = (f32x4){__uint_as_float(xv.z << 16), __uint_as_float(xv.z & 0xffff0000u), __uint_as_float(xv.w << 16), __uint_as_float(xv.w & 0xffff0000u)};
;                 const f32x4 v0 = x0 + gv[bj][0] * acc[ai][bj][m][0], v1 = x1 + gv[bj][1] * acc[ai][bj][m][1];
;                 u32x4 w; w.x = pg8::cvt_pk_bf16(v0[0], v0[1]); w.y = pg8::cvt_pk_bf16(v0[2], v0[3]); w.z = pg8::cvt_pk_bf16(v1[0], v1[1]); w.w = pg8::cvt_pk_bf16(v1[2], v1[3]);
;                 *(u32x4*)(out + EO_OFF(it)) = w;
;             }
	v_lshlrev_b32_e32 v232, 16, v212
	v_and_b32_e32 v233, 0xffff0000, v212
	v_lshlrev_b32_e32 v234, 16, v213
	v_and_b32_e32 v235, 0xffff0000, v213
	v_lshlrev_b32_e32 v244, 16, v214
	v_and_b32_e32 v245, 0xffff0000, v214
	v_lshlrev_b32_e32 v246, 16, v215
	v_and_b32_e32 v247, 0xffff0000, v215
	v_pk_fma_f32 v[40:41], v[40:41], v[56:57], v[232:233]
	v_pk_fma_f32 v[42:43], v[42:43], v[58:59], v[234:235]
	v_pk_fma_f32 v[36:37], v[36:37], v[52:53], v[244:245]
	v_pk_fma_f32 v[38:39], v[38:39], v[54:55], v[246:247]
	v_cvt_pk_bf16_f32 v212, v40, v41
	v_cvt_pk_bf16_f32 v213, v42, v43
	v_cvt_pk_bf16_f32 v214, v36, v37
	v_cvt_pk_bf16_f32 v215, v38, v39
	global_store_dwordx4 v207, v[212:215], s[32:33] offset:256
	s_add_u32 s32, s26, 0x50000
	s_addc_u32 s33, s27, 0
	s_waitcnt vmcnt(15)
	v_lshlrev_b32_e32 v232, 16, v216
	v_and_b32_e32 v233, 0xffff0000, v216
	v_lshlrev_b32_e32 v234, 16, v217
	v_and_b32_e32 v235, 0xffff0000, v217
	v_lshlrev_b32_e32 v244, 16, v218
	v_and_b32_e32 v245, 0xffff0000, v218
	v_lshlrev_b32_e32 v246, 16, v219
	v_and_b32_e32 v247, 0xffff0000, v219
	v_pk_fma_f32 v[30:31], v[30:31], v[64:65], v[232:233]
	v_pk_fma_f32 v[32:33], v[32:33], v[66:67], v[234:235]
	v_pk_fma_f32 v[26:27], v[26:27], v[60:61], v[244:245]
	v_pk_fma_f32 v[28:29], v[28:29], v[62:63], v[246:247]
	v_cvt_pk_bf16_f32 v216, v30, v31
	v_cvt_pk_bf16_f32 v217, v32, v33
	v_cvt_pk_bf16_f32 v218, v26, v27
	v_cvt_pk_bf16_f32 v219, v28, v29
	global_store_dwordx4 v207, v[216:219], s[32:33]
	s_waitcnt vmcnt(15)
	v_lshlrev_b32_e32 v232, 16, v220
	v_and_b32_e32 v233, 0xffff0000, v220
	v_lshlrev_b32_e32 v234, 16, v221
	v_and_b32_e32 v235, 0xffff0000, v221
	v_lshlrev_b32_e32 v244, 16, v222
	v_and_b32_e32 v245, 0xffff0000, v222
	v_lshlrev_b32_e32 v246, 16, v223
	v_and_b32_e32 v247, 0xffff0000, v223
	v_pk_fma_f32 v[22:23], v[22:23], v[56:57], v[232:233]
	v_pk_fma_f32 v[24:25], v[24:25], v[58:59], v[234:235]
	v_pk_fma_f32 v[18:19], v[18:19], v[52:53], v[244:245]
	v_pk_fma_f32 v[20:21], v[20:21], v[54:55], v[246:247]
	v_cvt_pk_bf16_f32 v220, v22, v23
	v_cvt_pk_bf16_f32 v221, v24, v25
	v_cvt_pk_bf16_f32 v222, v18, v19
	v_cvt_pk_bf16_f32 v223, v20, v21
	global_store_dwordx4 v207, v[220:223], s[32:33] offset:256
	s_add_u32 s32, s26, 0x58000
	s_addc_u32 s33, s27, 0
	s_waitcnt vmcnt(15)
	v_lshlrev_b32_e32 v232, 16, v224
	v_and_b32_e32 v233, 0xffff0000, v224
	v_lshlrev_b32_e32 v234, 16, v225
	v_and_b32_e32 v235, 0xffff0000, v225
	v_lshlrev_b32_e32 v244, 16, v226
	v_and_b32_e32 v245, 0xffff0000, v226
	v_lshlrev_b32_e32 v246, 16, v227
	v_and_b32_e32 v247, 0xffff0000, v227
	v_pk_fma_f32 v[14:15], v[14:15], v[64:65], v[232:233]
	v_pk_fma_f32 v[16:17], v[16:17], v[66:67], v[234:235]
	v_pk_fma_f32 v[10:11], v[10:11], v[60:61], v[244:245]
	v_pk_fma_f32 v[12:13], v[12:13], v[62:63], v[246:247]
	v_cvt_pk_bf16_f32 v224, v14, v15
	v_cvt_pk_bf16_f32 v225, v16, v17
	v_cvt_pk_bf16_f32 v226, v10, v11
	v_cvt_pk_bf16_f32 v227, v12, v13
	global_store_dwordx4 v207, v[224:227], s[32:33]
	s_waitcnt vmcnt(15)
	v_lshlrev_b32_e32 v232, 16, v228
	v_and_b32_e32 v233, 0xffff0000, v228
	v_lshlrev_b32_e32 v234, 16, v229
	v_and_b32_e32 v235, 0xffff0000, v229
	v_lshlrev_b32_e32 v244, 16, v230
	v_and_b32_e32 v245, 0xffff0000, v230
	v_lshlrev_b32_e32 v246, 16, v231
	v_and_b32_e32 v247, 0xffff0000, v231
	v_pk_fma_f32 v[6:7], v[6:7], v[56:57], v[232:233]
	v_pk_fma_f32 v[8:9], v[8:9], v[58:59], v[234:235]
	v_pk_fma_f32 v[2:3], v[2:3], v[52:53], v[244:245]
	v_pk_fma_f32 v[4:5], v[4:5], v[54:55], v[246:247]
	v_cvt_pk_bf16_f32 v228, v6, v7
	v_cvt_pk_bf16_f32 v229, v8, v9
	v_cvt_pk_bf16_f32 v230, v2, v3
	v_cvt_pk_bf16_f32 v231, v4, v5
	global_store_dwordx4 v207, v[228:231], s[32:33] offset:256
.Lop_epi_done:
	s_andn2_b64 vcc, exec, s[4:5]
	s_mov_b64 s[4:5], -1
	s_cbranch_vccnz .LBB0_709
	s_andn2_b64 vcc, exec, s[6:7]
	s_cbranch_vccnz .LBB0_708
	s_barrier
	s_branch .LBB0_708
